# P10 combine: the expert-output row loads (read once) and the final output stores (never re-read) carry the nt streaming hint
# speedup vs baseline: 1.0145x; 1.0047x over previous
.LBB0_1734:
	v_ashrrev_i32_e32 v73, 31, v72
	v_ashrrev_i32_e32 v67, 31, v66
	v_lshl_add_u64 v[80:81], v[72:73], 2, s[8:9]
	v_lshlrev_b64 v[82:83], 12, v[66:67]
	global_load_dword v100, v[80:81], off sc1
	global_load_dword v102, v[80:81], off offset:4 sc1
	global_load_dword v104, v[80:81], off offset:8 sc1
	global_load_dword v106, v[80:81], off offset:12 sc1
	global_load_dword v108, v[80:81], off offset:16 sc1
	global_load_dword v110, v[80:81], off offset:20 sc1
	global_load_dword v112, v[80:81], off offset:24 sc1
	global_load_dword v114, v[80:81], off offset:28 sc1
	v_lshlrev_b64 v[84:85], 13, v[66:67]
	v_lshl_add_u64 v[80:81], v[70:71], 0, v[82:83]
	v_lshl_add_u64 v[124:125], s[10:11], 0, v[84:85]
	global_load_dwordx4 v[84:87], v[80:81], off offset:3072
	global_load_dwordx4 v[88:91], v[80:81], off
	global_load_dwordx4 v[92:95], v[80:81], off offset:1024
	global_load_dwordx4 v[96:99], v[80:81], off offset:2048
	v_add_u32_e32 v78, v116, v66
	v_ashrrev_i32_e32 v79, 31, v78
	v_lshlrev_b64 v[78:79], 11, v[78:79]
	v_mov_b32_e32 v75, v65
	v_mov_b32_e32 v77, v65
	v_lshl_add_u64 v[126:127], v[68:69], 0, v[78:79]
	v_lshl_add_u64 v[82:83], v[124:125], 0, v[64:65]
	v_lshl_add_u64 v[80:81], v[124:125], 0, v[74:75]
	v_lshl_add_u64 v[78:79], v[124:125], 0, v[76:77]
	global_load_dwordx2 v[124:125], v[126:127], off nt
	global_load_dwordx2 v[128:129], v[126:127], off offset:512 nt
	global_load_dwordx2 v[130:131], v[126:127], off offset:1024 nt
	global_load_dwordx2 v[132:133], v[126:127], off offset:1536 nt
	v_add_u32_e32 v66, s5, v66
	v_cmp_lt_i32_e32 vcc, s7, v66
	s_or_b64 s[0:1], vcc, s[0:1]
	v_add_u32_e32 v72, s3, v72
	s_waitcnt vmcnt(15)
	v_ashrrev_i32_e32 v101, 31, v100
	s_waitcnt vmcnt(14)
	v_ashrrev_i32_e32 v103, 31, v102
	s_waitcnt vmcnt(13)
	v_ashrrev_i32_e32 v105, 31, v104
	s_waitcnt vmcnt(12)
	v_ashrrev_i32_e32 v107, 31, v106
	s_waitcnt vmcnt(11)
	v_ashrrev_i32_e32 v109, 31, v108
	s_waitcnt vmcnt(10)
	v_ashrrev_i32_e32 v111, 31, v110
	s_waitcnt vmcnt(9)
	v_ashrrev_i32_e32 v113, 31, v112
	s_waitcnt vmcnt(8)
	v_ashrrev_i32_e32 v115, 31, v114
	v_lshlrev_b64 v[100:101], 11, v[100:101]
	v_lshlrev_b64 v[102:103], 11, v[102:103]
	v_lshlrev_b64 v[104:105], 11, v[104:105]
	v_lshlrev_b64 v[106:107], 11, v[106:107]
	v_lshlrev_b64 v[108:109], 11, v[108:109]
	v_lshlrev_b64 v[110:111], 11, v[110:111]
	v_lshlrev_b64 v[112:113], 11, v[112:113]
	v_lshlrev_b64 v[114:115], 11, v[114:115]
	s_waitcnt vmcnt(7)
	v_and_b32_e32 v127, 0xffff0000, v86
	v_lshlrev_b32_e32 v126, 16, v86
	v_and_b32_e32 v135, 0xffff0000, v87
	v_lshlrev_b32_e32 v134, 16, v87
	s_waitcnt vmcnt(6)
	v_lshlrev_b32_e32 v136, 16, v90
	v_and_b32_e32 v137, 0xffff0000, v90
	v_lshlrev_b32_e32 v138, 16, v88
	v_and_b32_e32 v139, 0xffff0000, v88
	v_lshlrev_b32_e32 v140, 16, v89
	v_and_b32_e32 v141, 0xffff0000, v89
	s_waitcnt vmcnt(5)
	v_lshlrev_b32_e32 v142, 16, v94
	v_and_b32_e32 v143, 0xffff0000, v94
	v_lshlrev_b32_e32 v144, 16, v95
	v_and_b32_e32 v145, 0xffff0000, v95
	v_lshlrev_b32_e32 v146, 16, v92
	v_and_b32_e32 v147, 0xffff0000, v92
	v_lshlrev_b32_e32 v148, 16, v93
	v_and_b32_e32 v149, 0xffff0000, v93
	s_waitcnt vmcnt(4)
	v_lshlrev_b32_e32 v150, 16, v98
	v_and_b32_e32 v151, 0xffff0000, v98
	v_lshlrev_b32_e32 v152, 16, v99
	v_and_b32_e32 v153, 0xffff0000, v99
	v_lshlrev_b32_e32 v154, 16, v96
	v_and_b32_e32 v155, 0xffff0000, v96
	v_lshlrev_b32_e32 v156, 16, v97
	v_and_b32_e32 v157, 0xffff0000, v97
	v_lshlrev_b32_e32 v158, 16, v84
	v_and_b32_e32 v159, 0xffff0000, v84
	v_lshlrev_b32_e32 v160, 16, v85
	v_and_b32_e32 v161, 0xffff0000, v85
	v_lshl_add_u64 v[186:187], v[68:69], 0, v[100:101]
	v_lshl_add_u64 v[188:189], v[68:69], 0, v[102:103]
	v_lshl_add_u64 v[190:191], v[68:69], 0, v[104:105]
	v_lshl_add_u64 v[192:193], v[68:69], 0, v[106:107]
	v_lshl_add_u64 v[194:195], v[68:69], 0, v[108:109]
	v_lshl_add_u64 v[196:197], v[68:69], 0, v[110:111]
	v_lshl_add_u64 v[198:199], v[68:69], 0, v[112:113]
	v_lshl_add_u64 v[200:201], v[68:69], 0, v[114:115]
	v_pk_mul_f32 v[84:85], v[126:127], s[4:5] op_sel_hi:[1,0]
	v_pk_mul_f32 v[86:87], v[134:135], s[4:5] op_sel_hi:[1,0]
	v_pk_mul_f32 v[88:89], v[136:137], s[4:5] op_sel_hi:[1,0]
	v_pk_mul_f32 v[92:93], v[138:139], s[4:5] op_sel_hi:[1,0]
	v_pk_mul_f32 v[94:95], v[140:141], s[4:5] op_sel_hi:[1,0]
	v_pk_mul_f32 v[96:97], v[142:143], s[4:5] op_sel_hi:[1,0]
	v_pk_mul_f32 v[98:99], v[144:145], s[4:5] op_sel_hi:[1,0]
	v_pk_mul_f32 v[100:101], v[146:147], s[4:5] op_sel_hi:[1,0]
	v_pk_mul_f32 v[102:103], v[148:149], s[4:5] op_sel_hi:[1,0]
	v_pk_mul_f32 v[104:105], v[150:151], s[4:5] op_sel_hi:[1,0]
	v_pk_mul_f32 v[106:107], v[152:153], s[4:5] op_sel_hi:[1,0]
	v_pk_mul_f32 v[108:109], v[154:155], s[4:5] op_sel_hi:[1,0]
	v_pk_mul_f32 v[110:111], v[156:157], s[4:5] op_sel_hi:[1,0]
	v_pk_mul_f32 v[112:113], v[158:159], s[4:5] op_sel_hi:[1,0]
	v_pk_mul_f32 v[114:115], v[160:161], s[4:5] op_sel_hi:[1,0]
	global_load_dwordx2 v[126:127], v[186:187], off nt
	global_load_dwordx2 v[134:135], v[186:187], off offset:512 nt
	global_load_dwordx2 v[136:137], v[186:187], off offset:1024 nt
	global_load_dwordx2 v[138:139], v[186:187], off offset:1536 nt
	global_load_dwordx2 v[140:141], v[188:189], off nt
	global_load_dwordx2 v[142:143], v[188:189], off offset:512 nt
	global_load_dwordx2 v[144:145], v[188:189], off offset:1024 nt
	global_load_dwordx2 v[146:147], v[188:189], off offset:1536 nt
	global_load_dwordx2 v[148:149], v[190:191], off nt
	global_load_dwordx2 v[150:151], v[190:191], off offset:512 nt
	global_load_dwordx2 v[152:153], v[190:191], off offset:1024 nt
	global_load_dwordx2 v[154:155], v[190:191], off offset:1536 nt
	global_load_dwordx2 v[156:157], v[192:193], off nt
	global_load_dwordx2 v[158:159], v[192:193], off offset:512 nt
	global_load_dwordx2 v[160:161], v[192:193], off offset:1024 nt
	global_load_dwordx2 v[186:187], v[192:193], off offset:1536 nt
	global_load_dwordx2 v[188:189], v[194:195], off nt
	global_load_dwordx2 v[190:191], v[194:195], off offset:512 nt
	s_nop 0
	global_load_dwordx2 v[192:193], v[194:195], off offset:1024 nt
	s_nop 0
	global_load_dwordx2 v[194:195], v[194:195], off offset:1536 nt
	s_nop 0
	global_load_dwordx2 v[202:203], v[196:197], off nt
	global_load_dwordx2 v[204:205], v[196:197], off offset:512 nt
	global_load_dwordx2 v[206:207], v[196:197], off offset:1024 nt
	s_nop 0
	global_load_dwordx2 v[196:197], v[196:197], off offset:1536 nt
	s_nop 0
	global_load_dwordx2 v[208:209], v[198:199], off nt
	global_load_dwordx2 v[210:211], v[198:199], off offset:512 nt
	global_load_dwordx2 v[212:213], v[198:199], off offset:1024 nt
	s_nop 0
	global_load_dwordx2 v[198:199], v[198:199], off offset:1536 nt
	s_nop 0
	global_load_dwordx2 v[214:215], v[200:201], off nt
	global_load_dwordx2 v[216:217], v[200:201], off offset:512 nt
	global_load_dwordx2 v[218:219], v[200:201], off offset:1024 nt
	s_nop 0
	global_load_dwordx2 v[200:201], v[200:201], off offset:1536 nt
	s_waitcnt vmcnt(35)
	v_cvt_pk_f32_fp8_e32 v[162:163], v124
	v_cvt_pk_f32_fp8_sdwa v[164:165], v124 src0_sel:WORD_1
	v_cvt_pk_f32_fp8_e32 v[166:167], v125
	v_cvt_pk_f32_fp8_sdwa v[124:125], v125 src0_sel:WORD_1
	s_waitcnt vmcnt(34)
	v_cvt_pk_f32_fp8_e32 v[168:169], v128
	v_cvt_pk_f32_fp8_sdwa v[170:171], v128 src0_sel:WORD_1
	v_cvt_pk_f32_fp8_e32 v[172:173], v129
	v_cvt_pk_f32_fp8_sdwa v[128:129], v129 src0_sel:WORD_1
	s_waitcnt vmcnt(33)
	v_cvt_pk_f32_fp8_e32 v[174:175], v130
	v_cvt_pk_f32_fp8_sdwa v[176:177], v130 src0_sel:WORD_1
	v_cvt_pk_f32_fp8_e32 v[178:179], v131
	v_cvt_pk_f32_fp8_sdwa v[130:131], v131 src0_sel:WORD_1
	s_waitcnt vmcnt(32)
	v_cvt_pk_f32_fp8_e32 v[180:181], v132
	v_cvt_pk_f32_fp8_sdwa v[182:183], v132 src0_sel:WORD_1
	v_cvt_pk_f32_fp8_e32 v[184:185], v133
	v_cvt_pk_f32_fp8_sdwa v[132:133], v133 src0_sel:WORD_1
	v_pk_add_f32 v[162:163], v[162:163], 0 op_sel_hi:[1,0]
	v_pk_add_f32 v[164:165], v[164:165], 0 op_sel_hi:[1,0]
	v_pk_add_f32 v[166:167], v[166:167], 0 op_sel_hi:[1,0]
	v_pk_add_f32 v[124:125], v[124:125], 0 op_sel_hi:[1,0]
	v_pk_add_f32 v[168:169], v[168:169], 0 op_sel_hi:[1,0]
	v_pk_add_f32 v[170:171], v[170:171], 0 op_sel_hi:[1,0]
	v_pk_add_f32 v[172:173], v[172:173], 0 op_sel_hi:[1,0]
	v_pk_add_f32 v[128:129], v[128:129], 0 op_sel_hi:[1,0]
	v_pk_add_f32 v[174:175], v[174:175], 0 op_sel_hi:[1,0]
	v_pk_add_f32 v[176:177], v[176:177], 0 op_sel_hi:[1,0]
	v_pk_add_f32 v[130:131], v[130:131], 0 op_sel_hi:[1,0]
	v_pk_add_f32 v[180:181], v[180:181], 0 op_sel_hi:[1,0]
	v_pk_add_f32 v[182:183], v[182:183], 0 op_sel_hi:[1,0]
	v_pk_add_f32 v[184:185], v[184:185], 0 op_sel_hi:[1,0]
	v_pk_add_f32 v[132:133], v[132:133], 0 op_sel_hi:[1,0]
	v_pk_add_f32 v[178:179], v[178:179], 0 op_sel_hi:[1,0]
	v_lshlrev_b32_e32 v90, 16, v91
	v_and_b32_e32 v91, 0xffff0000, v91
	v_pk_mul_f32 v[90:91], v[90:91], s[4:5] op_sel_hi:[1,0]
	s_waitcnt vmcnt(31)
	v_cvt_pk_f32_fp8_e32 v[220:221], v126
	v_cvt_pk_f32_fp8_sdwa v[222:223], v126 src0_sel:WORD_1
	v_cvt_pk_f32_fp8_e32 v[224:225], v127
	v_cvt_pk_f32_fp8_sdwa v[126:127], v127 src0_sel:WORD_1
	s_waitcnt vmcnt(30)
	v_cvt_pk_f32_fp8_e32 v[226:227], v134
	v_cvt_pk_f32_fp8_sdwa v[228:229], v134 src0_sel:WORD_1
	v_cvt_pk_f32_fp8_e32 v[230:231], v135
	v_cvt_pk_f32_fp8_sdwa v[134:135], v135 src0_sel:WORD_1
	s_waitcnt vmcnt(29)
	v_cvt_pk_f32_fp8_e32 v[232:233], v136
	v_cvt_pk_f32_fp8_sdwa v[234:235], v136 src0_sel:WORD_1
	v_cvt_pk_f32_fp8_e32 v[236:237], v137
	v_cvt_pk_f32_fp8_sdwa v[136:137], v137 src0_sel:WORD_1
	s_waitcnt vmcnt(28)
	v_cvt_pk_f32_fp8_e32 v[238:239], v138
	v_cvt_pk_f32_fp8_sdwa v[240:241], v138 src0_sel:WORD_1
	v_cvt_pk_f32_fp8_e32 v[242:243], v139
	v_cvt_pk_f32_fp8_sdwa v[138:139], v139 src0_sel:WORD_1
	s_waitcnt vmcnt(27)
	v_cvt_pk_f32_fp8_e32 v[244:245], v140
	v_cvt_pk_f32_fp8_sdwa v[246:247], v140 src0_sel:WORD_1
	s_waitcnt vmcnt(26)
	v_cvt_pk_f32_fp8_e32 v[250:251], v142
	v_pk_add_f32 v[162:163], v[162:163], v[220:221]
	v_cvt_pk_f32_fp8_sdwa v[220:221], v142 src0_sel:WORD_1
	v_pk_add_f32 v[164:165], v[164:165], v[222:223]
	v_cvt_pk_f32_fp8_e32 v[222:223], v143
	v_cvt_pk_f32_fp8_sdwa v[142:143], v143 src0_sel:WORD_1
	v_pk_add_f32 v[166:167], v[166:167], v[224:225]
	s_waitcnt vmcnt(25)
	v_cvt_pk_f32_fp8_e32 v[224:225], v144
	v_pk_add_f32 v[124:125], v[124:125], v[126:127]
	v_cvt_pk_f32_fp8_sdwa v[126:127], v144 src0_sel:WORD_1
	v_cvt_pk_f32_fp8_e32 v[248:249], v141
	v_cvt_pk_f32_fp8_sdwa v[140:141], v141 src0_sel:WORD_1
	v_pk_add_f32 v[168:169], v[168:169], v[226:227]
	v_cvt_pk_f32_fp8_e32 v[226:227], v145
	v_cvt_pk_f32_fp8_sdwa v[144:145], v145 src0_sel:WORD_1
	v_pk_add_f32 v[170:171], v[170:171], v[228:229]
	s_waitcnt vmcnt(24)
	v_cvt_pk_f32_fp8_e32 v[228:229], v146
	v_pk_add_f32 v[172:173], v[172:173], v[230:231]
	v_cvt_pk_f32_fp8_sdwa v[230:231], v146 src0_sel:WORD_1
	v_pk_add_f32 v[128:129], v[128:129], v[134:135]
	v_cvt_pk_f32_fp8_e32 v[134:135], v147
	v_cvt_pk_f32_fp8_sdwa v[146:147], v147 src0_sel:WORD_1
	v_pk_add_f32 v[174:175], v[174:175], v[232:233]
	s_waitcnt vmcnt(23)
	v_cvt_pk_f32_fp8_e32 v[232:233], v148
	v_pk_add_f32 v[176:177], v[176:177], v[234:235]
	v_pk_add_f32 v[130:131], v[130:131], v[136:137]
	s_waitcnt vmcnt(22)
	v_cvt_pk_f32_fp8_e32 v[136:137], v150
	v_pk_add_f32 v[180:181], v[180:181], v[238:239]
	v_cvt_pk_f32_fp8_sdwa v[238:239], v150 src0_sel:WORD_1
	v_pk_add_f32 v[182:183], v[182:183], v[240:241]
	v_cvt_pk_f32_fp8_e32 v[240:241], v151
	v_cvt_pk_f32_fp8_sdwa v[150:151], v151 src0_sel:WORD_1
	v_pk_add_f32 v[184:185], v[184:185], v[242:243]
	s_waitcnt vmcnt(21)
	v_cvt_pk_f32_fp8_e32 v[242:243], v152
	v_pk_add_f32 v[132:133], v[132:133], v[138:139]
	v_cvt_pk_f32_fp8_sdwa v[138:139], v152 src0_sel:WORD_1
	v_pk_add_f32 v[162:163], v[162:163], v[244:245]
	v_cvt_pk_f32_fp8_e32 v[244:245], v153
	v_cvt_pk_f32_fp8_sdwa v[152:153], v153 src0_sel:WORD_1
	v_cvt_pk_f32_fp8_sdwa v[234:235], v148 src0_sel:WORD_1
	v_pk_add_f32 v[164:165], v[164:165], v[246:247]
	s_waitcnt vmcnt(20)
	v_cvt_pk_f32_fp8_e32 v[246:247], v154
	v_pk_add_f32 v[128:129], v[128:129], v[142:143]
	s_waitcnt vmcnt(18)
	v_cvt_pk_f32_fp8_e32 v[142:143], v158
	v_pk_add_f32 v[174:175], v[174:175], v[224:225]
	v_cvt_pk_f32_fp8_sdwa v[224:225], v158 src0_sel:WORD_1
	v_pk_add_f32 v[126:127], v[176:177], v[126:127]
	v_cvt_pk_f32_fp8_e32 v[176:177], v159
	v_cvt_pk_f32_fp8_sdwa v[158:159], v159 src0_sel:WORD_1
	v_pk_add_f32 v[124:125], v[124:125], v[140:141]
	v_cvt_pk_f32_fp8_e32 v[140:141], v155
	v_pk_add_f32 v[168:169], v[168:169], v[250:251]
	v_cvt_pk_f32_fp8_e32 v[250:251], v156
	v_pk_add_f32 v[166:167], v[166:167], v[248:249]
	v_cvt_pk_f32_fp8_sdwa v[248:249], v154 src0_sel:WORD_1
	v_pk_add_f32 v[130:131], v[130:131], v[144:145]
	v_pk_add_f32 v[132:133], v[132:133], v[146:147]
	s_waitcnt vmcnt(16)
	v_cvt_pk_f32_fp8_e32 v[146:147], v187
	v_pk_add_f32 v[162:163], v[162:163], v[232:233]
	s_waitcnt vmcnt(15)
	v_cvt_pk_f32_fp8_e32 v[232:233], v188
	v_pk_add_f32 v[178:179], v[178:179], v[236:237]
	v_cvt_pk_f32_fp8_e32 v[236:237], v149
	v_pk_add_f32 v[170:171], v[170:171], v[220:221]
	v_cvt_pk_f32_fp8_sdwa v[220:221], v156 src0_sel:WORD_1
	v_pk_add_f32 v[180:181], v[180:181], v[228:229]
	v_pk_add_f32 v[128:129], v[128:129], v[150:151]
	v_pk_add_f32 v[130:131], v[130:131], v[152:153]
	s_waitcnt vmcnt(12)
	v_cvt_pk_f32_fp8_e32 v[152:153], v195
	v_pk_add_f32 v[134:135], v[184:185], v[134:135]
	v_pk_add_f32 v[164:165], v[164:165], v[234:235]
	v_cvt_pk_f32_fp8_sdwa v[234:235], v188 src0_sel:WORD_1
	v_pk_add_f32 v[136:137], v[168:169], v[136:137]
	v_pk_add_f32 v[180:181], v[180:181], v[246:247]
	s_waitcnt vmcnt(11)
	v_cvt_pk_f32_fp8_e32 v[246:247], v202
	v_pk_add_f32 v[128:129], v[128:129], v[158:159]
	s_waitcnt vmcnt(8)
	v_cvt_pk_f32_fp8_e32 v[158:159], v197
	v_cvt_pk_f32_fp8_e32 v[228:229], v161
	v_pk_add_f32 v[182:183], v[182:183], v[230:231]
	v_pk_add_f32 v[134:135], v[134:135], v[140:141]
	v_pk_add_f32 v[162:163], v[162:163], v[250:251]
	v_pk_add_f32 v[136:137], v[136:137], v[142:143]
	s_waitcnt vmcnt(7)
	v_cvt_pk_f32_fp8_e32 v[142:143], v208
	v_cvt_pk_f32_fp8_sdwa v[148:149], v149 src0_sel:WORD_1
	v_pk_add_f32 v[172:173], v[172:173], v[222:223]
	v_cvt_pk_f32_fp8_e32 v[222:223], v157
	v_pk_add_f32 v[170:171], v[170:171], v[238:239]
	v_cvt_pk_f32_fp8_e32 v[238:239], v191
	v_pk_add_f32 v[182:183], v[182:183], v[248:249]
	v_cvt_pk_f32_fp8_sdwa v[248:249], v202 src0_sel:WORD_1
	v_pk_add_f32 v[134:135], v[134:135], v[146:147]
	v_pk_add_f32 v[162:163], v[162:163], v[232:233]
	s_waitcnt vmcnt(3)
	v_cvt_pk_f32_fp8_e32 v[232:233], v214
	v_pk_add_f32 v[178:179], v[178:179], v[226:227]
	v_pk_add_f32 v[166:167], v[166:167], v[236:237]
	v_cvt_pk_f32_fp8_e32 v[236:237], v189
	v_pk_add_f32 v[164:165], v[164:165], v[220:221]
	v_pk_add_f32 v[170:171], v[170:171], v[224:225]
	v_cvt_pk_f32_fp8_sdwa v[224:225], v208 src0_sel:WORD_1
	v_pk_add_f32 v[134:135], v[134:135], v[152:153]
	v_cvt_pk_f32_fp8_sdwa v[154:155], v155 src0_sel:WORD_1
	v_cvt_pk_f32_fp8_sdwa v[156:157], v157 src0_sel:WORD_1
	v_pk_add_f32 v[172:173], v[172:173], v[240:241]
	v_pk_add_f32 v[178:179], v[178:179], v[244:245]
	v_cvt_pk_f32_fp8_e32 v[140:141], v203
	v_pk_add_f32 v[164:165], v[164:165], v[234:235]
	v_cvt_pk_f32_fp8_sdwa v[234:235], v214 src0_sel:WORD_1
	v_pk_add_f32 v[134:135], v[134:135], v[158:159]
	v_pk_add_f32 v[158:159], v[162:163], v[246:247]
	v_cvt_pk_f32_fp8_e32 v[226:227], v160
	v_cvt_pk_f32_fp8_sdwa v[144:145], v160 src0_sel:WORD_1
	v_cvt_pk_f32_fp8_sdwa v[160:161], v161 src0_sel:WORD_1
	v_cvt_pk_f32_fp8_sdwa v[188:189], v189 src0_sel:WORD_1
	v_pk_add_f32 v[172:173], v[172:173], v[176:177]
	v_pk_add_f32 v[178:179], v[178:179], v[228:229]
	v_cvt_pk_f32_fp8_e32 v[228:229], v209
	v_pk_add_f32 v[142:143], v[158:159], v[142:143]
	v_pk_add_f32 v[124:125], v[124:125], v[148:149]
	v_cvt_pk_f32_fp8_e32 v[148:149], v190
	v_cvt_pk_f32_fp8_sdwa v[168:169], v190 src0_sel:WORD_1
	v_cvt_pk_f32_fp8_sdwa v[190:191], v191 src0_sel:WORD_1
	v_cvt_pk_f32_fp8_sdwa v[202:203], v203 src0_sel:WORD_1
	v_pk_add_f32 v[166:167], v[166:167], v[222:223]
	v_pk_add_f32 v[172:173], v[172:173], v[238:239]
	v_cvt_pk_f32_fp8_e32 v[238:239], v215
	v_pk_add_f32 v[162:163], v[164:165], v[248:249]
	v_pk_add_f32 v[142:143], v[142:143], v[232:233]
	v_cvt_pk_f32_fp8_sdwa v[208:209], v209 src0_sel:WORD_1
	v_pk_add_f32 v[166:167], v[166:167], v[236:237]
	v_pk_add_f32 v[158:159], v[162:163], v[224:225]
	v_pk_fma_f32 v[92:93], v[142:143], s[2:3], v[92:93] op_sel_hi:[1,0,1]
	v_cvt_pk_f32_fp8_e32 v[230:231], v186
	v_cvt_pk_f32_fp8_sdwa v[184:185], v186 src0_sel:WORD_1
	v_cvt_pk_f32_fp8_sdwa v[186:187], v187 src0_sel:WORD_1
	v_pk_add_f32 v[132:133], v[132:133], v[154:155]
	v_cvt_pk_f32_fp8_e32 v[154:155], v204
	v_pk_add_f32 v[124:125], v[124:125], v[156:157]
	v_cvt_pk_f32_fp8_sdwa v[214:215], v215 src0_sel:WORD_1
	v_pk_add_f32 v[140:141], v[166:167], v[140:141]
	v_pk_add_f32 v[158:159], v[158:159], v[234:235]
	v_add_f32_e32 v67, 0, v92
	v_pk_add_f32 v[130:131], v[130:131], v[160:161]
	v_cvt_pk_f32_fp8_e32 v[160:161], v210
	v_pk_add_f32 v[124:125], v[124:125], v[188:189]
	v_pk_add_f32 v[140:141], v[140:141], v[228:229]
	v_pk_fma_f32 v[94:95], v[158:159], s[2:3], v[94:95] op_sel_hi:[1,0,1]
	v_add_f32_e32 v67, v93, v67
	v_pk_add_f32 v[174:175], v[174:175], v[242:243]
	v_cvt_pk_f32_fp8_sdwa v[146:147], v204 src0_sel:WORD_1
	v_pk_add_f32 v[128:129], v[128:129], v[190:191]
	s_waitcnt vmcnt(2)
	v_cvt_pk_f32_fp8_e32 v[190:191], v216
	v_pk_add_f32 v[124:125], v[124:125], v[202:203]
	v_pk_add_f32 v[140:141], v[140:141], v[238:239]
	v_add_f32_e32 v67, v94, v67
	v_pk_add_f32 v[174:175], v[174:175], v[226:227]
	v_cvt_pk_f32_fp8_sdwa v[226:227], v210 src0_sel:WORD_1
	v_pk_add_f32 v[136:137], v[136:137], v[148:149]
	v_pk_add_f32 v[124:125], v[124:125], v[208:209]
	v_pk_fma_f32 v[88:89], v[140:141], s[2:3], v[88:89] op_sel_hi:[1,0,1]
	v_add_f32_e32 v67, v95, v67
	v_pk_add_f32 v[126:127], v[126:127], v[138:139]
	v_pk_add_f32 v[132:133], v[132:133], v[186:187]
	v_cvt_pk_f32_fp8_e32 v[186:187], v205
	v_cvt_pk_f32_fp8_sdwa v[148:149], v216 src0_sel:WORD_1
	v_pk_add_f32 v[136:137], v[136:137], v[154:155]
	v_pk_add_f32 v[124:125], v[124:125], v[214:215]
	v_add_f32_e32 v67, v88, v67
	v_pk_add_f32 v[126:127], v[126:127], v[144:145]
	v_cvt_pk_f32_fp8_e32 v[144:145], v211
	v_pk_add_f32 v[168:169], v[170:171], v[168:169]
	v_pk_add_f32 v[136:137], v[136:137], v[160:161]
	v_pk_fma_f32 v[90:91], v[124:125], s[2:3], v[90:91] op_sel_hi:[1,0,1]
	v_add_f32_e32 v67, v89, v67
	v_cvt_pk_f32_fp8_e32 v[240:241], v192
	v_cvt_pk_f32_fp8_e32 v[242:243], v193
	v_cvt_pk_f32_fp8_sdwa v[204:205], v205 src0_sel:WORD_1
	v_cvt_pk_f32_fp8_e32 v[170:171], v217
	v_pk_add_f32 v[146:147], v[168:169], v[146:147]
	v_pk_add_f32 v[136:137], v[136:137], v[190:191]
	v_add_f32_e32 v67, v90, v67
	v_cvt_pk_f32_fp8_sdwa v[210:211], v211 src0_sel:WORD_1
	v_pk_add_f32 v[146:147], v[146:147], v[226:227]
	v_pk_fma_f32 v[100:101], v[136:137], s[2:3], v[100:101] op_sel_hi:[1,0,1]
	v_add_f32_e32 v67, v91, v67
	v_cvt_pk_f32_fp8_sdwa v[150:151], v192 src0_sel:WORD_1
	v_cvt_pk_f32_fp8_sdwa v[192:193], v193 src0_sel:WORD_1
	v_cvt_pk_f32_fp8_e32 v[222:223], v206
	v_cvt_pk_f32_fp8_e32 v[250:251], v207
	v_cvt_pk_f32_fp8_sdwa v[216:217], v217 src0_sel:WORD_1
	v_pk_add_f32 v[164:165], v[172:173], v[186:187]
	v_pk_add_f32 v[146:147], v[146:147], v[148:149]
	v_add_f32_e32 v67, v100, v67
	v_pk_add_f32 v[180:181], v[180:181], v[230:231]
	v_cvt_pk_f32_fp8_e32 v[230:231], v212
	v_cvt_pk_f32_fp8_e32 v[152:153], v213
	v_pk_add_f32 v[144:145], v[164:165], v[144:145]
	v_pk_fma_f32 v[102:103], v[146:147], s[2:3], v[102:103] op_sel_hi:[1,0,1]
	v_add_f32_e32 v67, v101, v67
	v_cvt_pk_f32_fp8_sdwa v[156:157], v206 src0_sel:WORD_1
	v_pk_add_f32 v[178:179], v[178:179], v[242:243]
	s_waitcnt vmcnt(1)
	v_cvt_pk_f32_fp8_e32 v[242:243], v218
	v_pk_add_f32 v[174:175], v[174:175], v[240:241]
	v_cvt_pk_f32_fp8_e32 v[240:241], v219
	v_pk_add_f32 v[128:129], v[128:129], v[204:205]
	v_pk_add_f32 v[144:145], v[144:145], v[170:171]
	v_add_f32_e32 v67, v102, v67
	v_pk_add_f32 v[182:183], v[182:183], v[184:185]
	v_cvt_pk_f32_fp8_sdwa v[184:185], v212 src0_sel:WORD_1
	v_pk_add_f32 v[128:129], v[128:129], v[210:211]
	v_pk_fma_f32 v[96:97], v[144:145], s[2:3], v[96:97] op_sel_hi:[1,0,1]
	v_add_f32_e32 v67, v103, v67
	v_pk_add_f32 v[130:131], v[130:131], v[192:193]
	v_cvt_pk_f32_fp8_sdwa v[192:193], v218 src0_sel:WORD_1
	v_pk_add_f32 v[154:155], v[178:179], v[250:251]
	v_pk_add_f32 v[166:167], v[174:175], v[222:223]
	v_pk_add_f32 v[128:129], v[128:129], v[216:217]
	v_add_f32_e32 v67, v96, v67
	v_cvt_pk_f32_fp8_e32 v[138:139], v194
	v_cvt_pk_f32_fp8_sdwa v[244:245], v194 src0_sel:WORD_1
	v_cvt_pk_f32_fp8_sdwa v[194:195], v195 src0_sel:WORD_1
	v_pk_add_f32 v[126:127], v[126:127], v[150:151]
	v_pk_add_f32 v[152:153], v[154:155], v[152:153]
	v_pk_add_f32 v[154:155], v[166:167], v[230:231]
	v_pk_fma_f32 v[98:99], v[128:129], s[2:3], v[98:99] op_sel_hi:[1,0,1]
	v_add_f32_e32 v67, v97, v67
	v_cvt_pk_f32_fp8_sdwa v[206:207], v207 src0_sel:WORD_1
	v_pk_add_f32 v[126:127], v[126:127], v[156:157]
	v_pk_add_f32 v[148:149], v[152:153], v[240:241]
	v_pk_add_f32 v[152:153], v[154:155], v[242:243]
	v_add_f32_e32 v67, v98, v67
	v_cvt_pk_f32_fp8_sdwa v[212:213], v213 src0_sel:WORD_1
	v_pk_add_f32 v[126:127], v[126:127], v[184:185]
	v_pk_fma_f32 v[108:109], v[152:153], s[2:3], v[108:109] op_sel_hi:[1,0,1]
	v_add_f32_e32 v67, v99, v67
	v_cvt_pk_f32_fp8_e32 v[220:221], v196
	v_cvt_pk_f32_fp8_sdwa v[218:219], v219 src0_sel:WORD_1
	v_pk_add_f32 v[126:127], v[126:127], v[192:193]
	v_add_f32_e32 v67, v108, v67
	v_pk_add_f32 v[132:133], v[132:133], v[194:195]
	v_cvt_pk_f32_fp8_e32 v[194:195], v198
	v_pk_fma_f32 v[110:111], v[126:127], s[2:3], v[110:111] op_sel_hi:[1,0,1]
	v_add_f32_e32 v67, v109, v67
	v_cvt_pk_f32_fp8_sdwa v[176:177], v196 src0_sel:WORD_1
	s_waitcnt vmcnt(0)
	v_cvt_pk_f32_fp8_e32 v[150:151], v200
	v_pk_add_f32 v[130:131], v[130:131], v[206:207]
	v_add_f32_e32 v67, v110, v67
	v_cvt_pk_f32_fp8_sdwa v[236:237], v198 src0_sel:WORD_1
	v_pk_add_f32 v[138:139], v[180:181], v[138:139]
	v_pk_add_f32 v[130:131], v[130:131], v[212:213]
	v_pk_fma_f32 v[104:105], v[148:149], s[2:3], v[104:105] op_sel_hi:[1,0,1]
	v_add_f32_e32 v67, v111, v67
	v_cvt_pk_f32_fp8_sdwa v[180:181], v200 src0_sel:WORD_1
	v_pk_add_f32 v[138:139], v[138:139], v[220:221]
	v_pk_add_f32 v[130:131], v[130:131], v[218:219]
	v_add_f32_e32 v67, v104, v67
	v_cvt_pk_f32_fp8_e32 v[188:189], v199
	v_pk_add_f32 v[182:183], v[182:183], v[244:245]
	v_pk_add_f32 v[138:139], v[138:139], v[194:195]
	v_pk_fma_f32 v[106:107], v[130:131], s[2:3], v[106:107] op_sel_hi:[1,0,1]
	v_add_f32_e32 v67, v105, v67
	v_cvt_pk_f32_fp8_sdwa v[196:197], v197 src0_sel:WORD_1
	v_cvt_pk_f32_fp8_e32 v[244:245], v201
	v_pk_add_f32 v[156:157], v[182:183], v[176:177]
	v_pk_add_f32 v[138:139], v[138:139], v[150:151]
	v_add_f32_e32 v67, v106, v67
	v_cvt_pk_f32_fp8_sdwa v[198:199], v199 src0_sel:WORD_1
	v_pk_add_f32 v[156:157], v[156:157], v[236:237]
	v_pk_fma_f32 v[112:113], v[138:139], s[2:3], v[112:113] op_sel_hi:[1,0,1]
	v_add_f32_e32 v67, v107, v67
	v_cvt_pk_f32_fp8_sdwa v[200:201], v201 src0_sel:WORD_1
	v_pk_add_f32 v[150:151], v[156:157], v[180:181]
	v_add_f32_e32 v67, v112, v67
	v_pk_add_f32 v[134:135], v[134:135], v[188:189]
	v_pk_fma_f32 v[114:115], v[150:151], s[2:3], v[114:115] op_sel_hi:[1,0,1]
	v_add_f32_e32 v67, v113, v67
	v_pk_add_f32 v[132:133], v[132:133], v[196:197]
	v_pk_add_f32 v[134:135], v[134:135], v[244:245]
	v_add_f32_e32 v67, v114, v67
	v_pk_add_f32 v[132:133], v[132:133], v[198:199]
	v_pk_fma_f32 v[84:85], v[134:135], s[2:3], v[84:85] op_sel_hi:[1,0,1]
	v_add_f32_e32 v67, v115, v67
	v_pk_add_f32 v[132:133], v[132:133], v[200:201]
	v_add_f32_e32 v67, v84, v67
	v_pk_fma_f32 v[86:87], v[132:133], s[2:3], v[86:87] op_sel_hi:[1,0,1]
	v_add_f32_e32 v67, v85, v67
	v_add_f32_e32 v67, v86, v67
	v_add_f32_e32 v67, v87, v67
	v_mov_b32_e32 v73, v67
	s_nop 1
	v_permlane32_swap_b32_e32 v73, v67
	s_waitcnt lgkmcnt(0)
	v_add_f32_e32 v67, v67, v73
	v_mov_b32_e32 v73, v67
	s_nop 1
	v_permlane16_swap_b32_e32 v73, v67
	s_waitcnt lgkmcnt(0)
	v_add_f32_e32 v67, v67, v73
	s_nop 1
	v_mov_b32_dpp v73, v67 row_ror:8 row_mask:0xf bank_mask:0xf
	s_waitcnt lgkmcnt(0)
	v_add_f32_e32 v67, v67, v73
	s_nop 1
	v_mov_b32_dpp v73, v67 row_shr:4 row_mask:0xf bank_mask:0xa
	v_mov_b32_dpp v73, v67 row_shl:4 row_mask:0xf bank_mask:0x5
	s_waitcnt lgkmcnt(0)
	v_add_f32_e32 v67, v67, v73
	s_nop 1
	v_mov_b32_dpp v73, v67 quad_perm:[2,3,0,1] row_mask:0xf bank_mask:0xf
	s_waitcnt lgkmcnt(0)
	v_add_f32_e32 v67, v67, v73
	s_nop 1
	v_mov_b32_dpp v73, v67 quad_perm:[1,0,3,2] row_mask:0xf bank_mask:0xf
	s_waitcnt lgkmcnt(0)
	v_add_f32_e32 v67, v67, v73
	v_mul_f32_e32 v124, 0x3a000000, v67
	v_pk_add_f32 v[92:93], v[92:93], v[124:125] op_sel_hi:[1,0] neg_lo:[0,1] neg_hi:[0,1]
	v_pk_add_f32 v[94:95], v[94:95], v[124:125] op_sel_hi:[1,0] neg_lo:[0,1] neg_hi:[0,1]
	v_pk_add_f32 v[88:89], v[88:89], v[124:125] op_sel_hi:[1,0] neg_lo:[0,1] neg_hi:[0,1]
	v_pk_add_f32 v[90:91], v[90:91], v[124:125] op_sel_hi:[1,0] neg_lo:[0,1] neg_hi:[0,1]
	v_pk_add_f32 v[100:101], v[100:101], v[124:125] op_sel_hi:[1,0] neg_lo:[0,1] neg_hi:[0,1]
	v_pk_add_f32 v[102:103], v[102:103], v[124:125] op_sel_hi:[1,0] neg_lo:[0,1] neg_hi:[0,1]
	v_pk_add_f32 v[96:97], v[96:97], v[124:125] op_sel_hi:[1,0] neg_lo:[0,1] neg_hi:[0,1]
	v_pk_add_f32 v[98:99], v[98:99], v[124:125] op_sel_hi:[1,0] neg_lo:[0,1] neg_hi:[0,1]
	v_pk_add_f32 v[108:109], v[108:109], v[124:125] op_sel_hi:[1,0] neg_lo:[0,1] neg_hi:[0,1]
	v_pk_add_f32 v[110:111], v[110:111], v[124:125] op_sel_hi:[1,0] neg_lo:[0,1] neg_hi:[0,1]
	v_pk_add_f32 v[104:105], v[104:105], v[124:125] op_sel_hi:[1,0] neg_lo:[0,1] neg_hi:[0,1]
	v_pk_add_f32 v[106:107], v[106:107], v[124:125] op_sel_hi:[1,0] neg_lo:[0,1] neg_hi:[0,1]
	v_pk_add_f32 v[112:113], v[112:113], v[124:125] op_sel_hi:[1,0] neg_lo:[0,1] neg_hi:[0,1]
	v_pk_add_f32 v[114:115], v[114:115], v[124:125] op_sel_hi:[1,0] neg_lo:[0,1] neg_hi:[0,1]
	v_pk_add_f32 v[84:85], v[84:85], v[124:125] op_sel_hi:[1,0] neg_lo:[0,1] neg_hi:[0,1]
	v_pk_add_f32 v[86:87], v[86:87], v[124:125] op_sel_hi:[1,0] neg_lo:[0,1] neg_hi:[0,1]
	v_pk_mul_f32 v[124:125], v[92:93], v[92:93]
	v_pk_mul_f32 v[126:127], v[94:95], v[94:95]
	v_add_f32_e32 v67, v124, v125
	v_add_f32_e32 v67, v126, v67
	v_pk_mul_f32 v[128:129], v[88:89], v[88:89]
	v_add_f32_e32 v67, v127, v67
	v_add_f32_e32 v67, v128, v67
	v_pk_mul_f32 v[130:131], v[90:91], v[90:91]
	v_add_f32_e32 v67, v129, v67
	v_add_f32_e32 v67, v130, v67
	v_pk_mul_f32 v[132:133], v[100:101], v[100:101]
	v_add_f32_e32 v67, v131, v67
	v_add_f32_e32 v67, v132, v67
	v_pk_mul_f32 v[134:135], v[102:103], v[102:103]
	v_add_f32_e32 v67, v133, v67
	v_add_f32_e32 v67, v134, v67
	v_pk_mul_f32 v[136:137], v[96:97], v[96:97]
	v_add_f32_e32 v67, v135, v67
	v_add_f32_e32 v67, v136, v67
	v_pk_mul_f32 v[138:139], v[98:99], v[98:99]
	v_add_f32_e32 v67, v137, v67
	v_add_f32_e32 v67, v138, v67
	v_pk_mul_f32 v[140:141], v[108:109], v[108:109]
	v_add_f32_e32 v67, v139, v67
	v_add_f32_e32 v67, v140, v67
	v_pk_mul_f32 v[142:143], v[110:111], v[110:111]
	v_add_f32_e32 v67, v141, v67
	v_add_f32_e32 v67, v142, v67
	v_pk_mul_f32 v[144:145], v[104:105], v[104:105]
	v_add_f32_e32 v67, v143, v67
	v_add_f32_e32 v67, v144, v67
	v_pk_mul_f32 v[146:147], v[106:107], v[106:107]
	v_add_f32_e32 v67, v145, v67
	v_add_f32_e32 v67, v146, v67
	v_pk_mul_f32 v[148:149], v[112:113], v[112:113]
	v_add_f32_e32 v67, v147, v67
	v_add_f32_e32 v67, v148, v67
	v_pk_mul_f32 v[150:151], v[114:115], v[114:115]
	v_add_f32_e32 v67, v149, v67
	v_add_f32_e32 v67, v150, v67
	v_pk_mul_f32 v[152:153], v[84:85], v[84:85]
	v_add_f32_e32 v67, v151, v67
	v_add_f32_e32 v67, v152, v67
	v_pk_mul_f32 v[154:155], v[86:87], v[86:87]
	v_add_f32_e32 v67, v153, v67
	v_add_f32_e32 v67, v154, v67
	v_add_f32_e32 v67, v155, v67
	v_mov_b32_e32 v73, v67
	s_nop 1
	v_permlane32_swap_b32_e32 v73, v67
	s_waitcnt lgkmcnt(0)
	v_add_f32_e32 v67, v67, v73
	v_mov_b32_e32 v73, v67
	s_nop 1
	v_permlane16_swap_b32_e32 v73, v67
	s_waitcnt lgkmcnt(0)
	v_add_f32_e32 v67, v67, v73
	s_nop 1
	v_mov_b32_dpp v73, v67 row_ror:8 row_mask:0xf bank_mask:0xf
	s_waitcnt lgkmcnt(0)
	v_add_f32_e32 v67, v67, v73
	s_nop 1
	v_mov_b32_dpp v73, v67 row_shr:4 row_mask:0xf bank_mask:0xa
	v_mov_b32_dpp v73, v67 row_shl:4 row_mask:0xf bank_mask:0x5
	s_waitcnt lgkmcnt(0)
	v_add_f32_e32 v67, v67, v73
	s_nop 1
	v_mov_b32_dpp v73, v67 quad_perm:[2,3,0,1] row_mask:0xf bank_mask:0xf
	s_waitcnt lgkmcnt(0)
	v_add_f32_e32 v67, v67, v73
	s_nop 1
	v_mov_b32_dpp v73, v67 quad_perm:[1,0,3,2] row_mask:0xf bank_mask:0xf
	s_waitcnt lgkmcnt(0)
	v_add_f32_e32 v67, v67, v73
	v_fmamk_f32 v67, v67, 0x3a000000, v123
	v_mul_f32_e32 v73, 0x4b800000, v67
	v_cmp_gt_f32_e32 vcc, s6, v67
	s_nop 1
	v_cndmask_b32_e32 v67, v67, v73, vcc
	v_rsq_f32_e32 v67, v67
	s_nop 0
	v_mul_f32_e32 v73, 0x45800000, v67
	v_cndmask_b32_e32 v124, v67, v73, vcc
	v_pk_mul_f32 v[92:93], v[92:93], v[124:125] op_sel_hi:[1,0]
	v_pk_mul_f32 v[94:95], v[94:95], v[124:125] op_sel_hi:[1,0]
	v_pk_mul_f32 v[88:89], v[88:89], v[124:125] op_sel_hi:[1,0]
	v_pk_mul_f32 v[90:91], v[90:91], v[124:125] op_sel_hi:[1,0]
	v_pk_mul_f32 v[100:101], v[100:101], v[124:125] op_sel_hi:[1,0]
	v_pk_mul_f32 v[102:103], v[102:103], v[124:125] op_sel_hi:[1,0]
	v_pk_mul_f32 v[96:97], v[96:97], v[124:125] op_sel_hi:[1,0]
	v_pk_mul_f32 v[98:99], v[98:99], v[124:125] op_sel_hi:[1,0]
	v_pk_mul_f32 v[108:109], v[108:109], v[124:125] op_sel_hi:[1,0]
	v_pk_mul_f32 v[110:111], v[110:111], v[124:125] op_sel_hi:[1,0]
	v_pk_mul_f32 v[104:105], v[104:105], v[124:125] op_sel_hi:[1,0]
	v_pk_mul_f32 v[106:107], v[106:107], v[124:125] op_sel_hi:[1,0]
	v_pk_mul_f32 v[112:113], v[112:113], v[124:125] op_sel_hi:[1,0]
	v_pk_mul_f32 v[114:115], v[114:115], v[124:125] op_sel_hi:[1,0]
	v_pk_mul_f32 v[126:127], v[84:85], v[124:125] op_sel_hi:[1,0]
	v_pk_mul_f32 v[124:125], v[86:87], v[124:125] op_sel_hi:[1,0]
	v_pk_fma_f32 v[86:87], v[62:63], v[94:95], v[58:59]
	v_pk_fma_f32 v[84:85], v[60:61], v[92:93], v[56:57]
	v_pk_fma_f32 v[90:91], v[54:55], v[90:91], v[50:51]
	v_pk_fma_f32 v[88:89], v[52:53], v[88:89], v[48:49]
	v_pk_fma_f32 v[94:95], v[46:47], v[102:103], v[42:43]
	v_pk_fma_f32 v[92:93], v[44:45], v[100:101], v[40:41]
	v_pk_fma_f32 v[98:99], v[38:39], v[98:99], v[34:35]
	v_pk_fma_f32 v[96:97], v[36:37], v[96:97], v[32:33]
	v_pk_fma_f32 v[102:103], v[30:31], v[110:111], v[26:27]
	v_pk_fma_f32 v[100:101], v[28:29], v[108:109], v[24:25]
	v_pk_fma_f32 v[106:107], v[22:23], v[106:107], v[18:19]
	v_pk_fma_f32 v[104:105], v[20:21], v[104:105], v[16:17]
	v_pk_fma_f32 v[110:111], v[14:15], v[114:115], v[10:11]
	v_pk_fma_f32 v[108:109], v[12:13], v[112:113], v[8:9]
	v_pk_fma_f32 v[114:115], v[6:7], v[124:125], v[2:3]
	v_pk_fma_f32 v[112:113], v[4:5], v[126:127], v[0:1]
	global_store_dwordx4 v[82:83], v[84:87], off nt
	global_store_dwordx4 v[82:83], v[88:91], off offset:16 nt
	global_store_dwordx4 v[82:83], v[92:95], off offset:2048 nt
	global_store_dwordx4 v[82:83], v[96:99], off offset:2064 nt
	global_store_dwordx4 v[80:81], v[100:103], off nt
	global_store_dwordx4 v[80:81], v[104:107], off offset:16 nt
	global_store_dwordx4 v[78:79], v[108:111], off nt
	global_store_dwordx4 v[78:79], v[112:115], off offset:16 nt
	s_andn2_b64 exec, exec, s[0:1]
	s_cbranch_execnz .LBB0_1734
